# split-phase SEAM(9) plus conversion share of the non-attention workgroups lowered from 24 to 22 of 28 items per wave pair
# baseline (speedup 1.0000x reference)
; #define LAS __attribute__((address_space(3)))
; __device__ __forceinline__ void convert_items(Frame& F, const Args& a, int lo, int hi, int w, int nw) {
;     const int lane = pg8::pg8_lane_id();
;     LAS float* scr = (LAS float*)(F.lds + RING_OFF + F.wave * 8448);
;     constexpr int I_FI = CONV_I_FI, I_FO = CONV_I_FO, I_SI = CONV_I_SI, I_SO = CONV_I_SO, I_GU = CONV_I_GU, I_DN = CONV_I_DN;
;     for (int it = lo + w; it < hi; it += nw) {
;         int r = it;
;         if (r < I_FI) { tr_item(a.in[7], 3 * D + 16, D, 96, r, (bf16*)(F.ws + WS_WFOXIN), false, scr, lane); continue; } r -= I_FI;
;         if (r < I_FO) { tr_item(a.in[9], D, D, 32, r, (bf16*)(F.ws + WS_WFOXOUT), false, scr, lane); continue; } r -= I_FO;
;         if (r < I_SI) { tr_item(a.in[10], D + 512, D, 48, r, (bf16*)(F.ws + WS_WSWAIN), false, scr, lane); continue; } r -= I_SI;
;         if (r < I_SO) { tr_item(a.in[12], D, D, 32, r, (bf16*)(F.ws + WS_WSWAOUT), false, scr, lane); continue; } r -= I_SO;
;         if (r < I_GU) { tr_item8(a.in[14], 2 * FF, D, 224, r, F.ws + WS_WGU, true, WSC_GU, scr, lane); continue; } r -= I_GU;
;         if (r < I_DN) { tr_item8(a.in[15], D, FF, 32, r, F.ws + WS_WDN, false, WSC_DN, scr, lane); continue; } r -= I_DN;
;         if (r < NE * I_GU) { const int e = r / I_GU, rr = r % I_GU; tr_item8(a.in[18] + (size_t)e * D * 2 * FF, 2 * FF, D, 224, rr, F.ws + WS_WMGU + (size_t)e * 2 * FF * D, true, WSC_GU, scr, lane); continue; } r -= NE * I_GU;
; __global__ void __launch_bounds__(NWAVES * 64, 2) mk_fwd(Args args) {
;     ...
;         if (F.G == 256 && rep_ == 0) {
;             constexpr int NODD = CONV_SWA_ODD * 128 * NWAVES; const int lo = CONV_NITEMS - CONV_SWA;
;             const int rank = F.c >> 3, xcc = F.c & 7;
;             const bool att = F.loc ? (rank < 16) : ((F.c & 1) == 0);
;             const int half = F.loc ? (xcc * 16 + (rank & 15)) : (F.c >> 1), w = half * NWAVES + F.wave;
;             const int run = F.loc ? ((xcc >> 1) * 32 + (rank & 3) * 8 + (xcc & 1) * 4 + ((rank >> 2) & 3)) : half;
;             if (att) { swa_phase((char*)lds + RING_OFF, QO, KB, VB, XN, args.in[11], args.in[13], (LAS float*)(F.lds + RING_OFF + 100 * 1024), run, 128, F.wave);
;                        convert_items(F, args, lo + NODD, CONV_NITEMS, w, 128 * NWAVES); }
;             else convert_items(F, args, lo, lo + NODD, w, 128 * NWAVES); }
.LBB0_1325:
	s_and_b64 vcc, exec, s[0:1]
	s_cbranch_vccz .LBB0_1434
	s_ashr_i32 s4, s2, 3
	s_lshl_b32 s10, s2, 4
	s_and_b32 s0, s10, 0x70
	s_and_b32 s1, s4, 15
	v_readlane_b32 s6, v254, 24
	s_or_b32 s3, s0, s1
	s_ashr_i32 s11, s2, 1
	v_readlane_b32 s7, v254, 25
	s_and_b64 s[0:1], s[6:7], exec
	s_cselect_b32 s0, s11, s3
	s_lshl_b32 s3, s0, 3
	v_readlane_b32 s0, v254, 3
	s_add_i32 s3, s3, s0
	s_bitcmp0_b32 s2, 0
	s_cselect_b64 s[0:1], -1, 0
	s_cmp_lt_i32 s4, 16
	s_cselect_b64 s[4:5], -1, 0
	v_cndmask_b32_e64 v0, 0, 1, s[4:5]
	s_waitcnt lgkmcnt(0)
	v_cndmask_b32_e64 v1, 0, 1, s[0:1]
	v_cndmask_b32_e64 v0, v0, v1, s[6:7]
	v_and_b32_e32 v0, 1, v0
	v_cmp_eq_u32_e32 vcc, 0, v0
	s_mov_b64 s[0:1], -1
	s_cbranch_vccz .LBB0_1359
	s_cmpk_gt_i32 s3, 0x57ff
	v_mbcnt_lo_u32_b32 v4, -1, 0
	v_mbcnt_hi_u32_b32 v4, -1, v4
	s_cbranch_scc1 .LBB0_1358
	v_ashrrev_i32_e32 v30, 5, v4
	v_and_b32_e32 v28, 31, v4
	s_movk_i32 s0, 0x84
	v_lshlrev_b32_e32 v0, 2, v28
	v_mul_lo_u32 v2, v30, s0
	v_add3_u32 v31, s56, v0, v2
	v_lshlrev_b32_e32 v2, 4, v4
	v_ashrrev_i32_e32 v32, 2, v4
	v_and_b32_e32 v2, 48, v2
	v_and_b32_e32 v6, -4, v4
	v_ashrrev_i32_e32 v35, 3, v4
	v_lshlrev_b32_e32 v4, 3, v4
	v_mul_u32_u24_e32 v5, 0x84, v2
	v_and_b32_e32 v20, 56, v4
	v_readlane_b32 s40, v254, 5
	v_mov_b32_e32 v1, 0
	v_add3_u32 v33, s56, v5, v6
	v_mul_u32_u24_e32 v4, 0x84, v20
	v_lshlrev_b32_e32 v5, 2, v35
	v_readlane_b32 s41, v254, 6
	v_readlane_b32 s42, v254, 7
	v_readlane_b32 s43, v254, 8
	v_readlane_b32 s44, v254, 9
	v_readlane_b32 s45, v254, 10
	v_readlane_b32 s46, v254, 11
	v_readlane_b32 s47, v254, 12
	v_readlane_b32 s48, v254, 13
	v_readlane_b32 s49, v254, 14
	v_readlane_b32 s50, v254, 15
	v_readlane_b32 s51, v254, 16
	v_readlane_b32 s52, v254, 17
	v_readlane_b32 s53, v254, 18
	v_readlane_b32 s54, v254, 19
	v_readlane_b32 s55, v254, 20
	v_add3_u32 v36, s56, v4, v5
	v_lshl_add_u64 v[6:7], s[52:53], 0, v[0:1]
	v_lshl_add_u64 v[4:5], s[54:55], 0, v[0:1]
	v_lshl_add_u64 v[8:9], s[48:49], 0, v[0:1]
	v_lshl_add_u64 v[10:11], s[44:45], 0, v[0:1]
	v_lshl_add_u64 v[12:13], s[42:43], 0, v[0:1]
	v_readlane_b32 s40, v254, 36
	s_add_i32 s8, s3, 0x5a00
	v_readlane_b32 s54, v254, 50
	v_readlane_b32 s55, v254, 51
	v_mov_b32_e32 v3, v1
	s_lshl_b32 s0, s8, 1
	v_lshl_add_u64 v[14:15], s[54:55], 0, v[0:1]
	v_lshlrev_b32_e32 v0, 1, v20
	v_add_u32_e32 v34, 16, v32
	v_add_u32_e32 v37, 8, v35
	v_add_u32_e32 v38, 16, v35
	v_add_u32_e32 v39, 24, v35
	v_lshl_add_u64 v[16:17], s[26:27], 0, v[2:3]
	v_lshl_add_u64 v[18:19], s[60:61], 0, v[2:3]
	v_lshl_add_u64 v[20:21], s[62:63], 0, v[0:1]
	v_lshl_add_u64 v[22:23], s[64:65], 0, v[0:1]
	v_lshl_add_u64 v[24:25], s[84:85], 0, v[0:1]
	v_lshl_add_u64 v[26:27], s[86:87], 0, v[0:1]
	s_lshl_b32 s9, s8, 5
	s_add_i32 s12, s0, 0x1ca00
	s_mov_b32 s1, 0
	s_movk_i32 s13, 0xe00
	s_movk_i32 s14, 0x7000
	s_movk_i32 s15, 0x7fff
	s_mov_b32 s16, 0xffff0000
	s_movk_i32 s17, 0x1800
	s_movk_i32 s30, 0x3040
	v_lshlrev_b32_e32 v0, 2, v28
	v_add_u32_e32 v40, 0x400, v31
	v_add_u32_e32 v41, 0x800, v31
	v_add_u32_e32 v42, 0xc00, v31
	v_add_u32_e32 v43, 0x1000, v31
	v_add_u32_e32 v44, 0x1400, v31
	v_add_u32_e32 v45, 0x1800, v31
	v_add_u32_e32 v46, 0x1c00, v31
	v_add_u32_e32 v47, 0x400, v33
	v_readlane_b32 s41, v254, 37
	v_readlane_b32 s42, v254, 38
	v_readlane_b32 s43, v254, 39
	v_readlane_b32 s44, v254, 40
	v_readlane_b32 s45, v254, 41
	v_readlane_b32 s46, v254, 42
	v_readlane_b32 s47, v254, 43
	v_readlane_b32 s48, v254, 44
	v_readlane_b32 s49, v254, 45
	v_readlane_b32 s50, v254, 46
	v_readlane_b32 s51, v254, 47
	v_readlane_b32 s52, v254, 48
	v_readlane_b32 s53, v254, 49
	s_branch .LBB0_1330
.LBB0_1329:
	s_add_i32 s0, s8, 0x400
	s_add_i32 s9, s9, 0x8000
	s_addk_i32 s12, 0x800
	s_cmp_gt_i32 s8, 0xadff
	s_mov_b32 s8, s0
	s_cbranch_scc1 .LBB0_1358

; __device__ __forceinline__ int pg8_lane_id() { int l; asm volatile("v_mbcnt_lo_u32_b32 %0, -1, 0\n\tv_mbcnt_hi_u32_b32 %0, -1, %0" : "=v"(l)); return l; }
; #define LAS __attribute__((address_space(3)))
; __device__ __forceinline__ void convert_items(Frame& F, const Args& a, int lo, int hi, int w, int nw) {
;     const int lane = pg8::pg8_lane_id();
;     LAS float* scr = (LAS float*)(F.lds + RING_OFF + F.wave * 8448);
;     constexpr int I_FI = CONV_I_FI, I_FO = CONV_I_FO, I_SI = CONV_I_SI, I_SO = CONV_I_SO, I_GU = CONV_I_GU, I_DN = CONV_I_DN;
;     for (int it = lo + w; it < hi; it += nw) {
;         int r = it;
;         if (r < I_FI) { tr_item(a.in[7], 3 * D + 16, D, 96, r, (bf16*)(F.ws + WS_WFOXIN), false, scr, lane); continue; } r -= I_FI;
;         if (r < I_FO) { tr_item(a.in[9], D, D, 32, r, (bf16*)(F.ws + WS_WFOXOUT), false, scr, lane); continue; } r -= I_FO;
;         if (r < I_SI) { tr_item(a.in[10], D + 512, D, 48, r, (bf16*)(F.ws + WS_WSWAIN), false, scr, lane); continue; } r -= I_SI;
;         if (r < I_SO) { tr_item(a.in[12], D, D, 32, r, (bf16*)(F.ws + WS_WSWAOUT), false, scr, lane); continue; } r -= I_SO;
;         if (r < I_GU) { tr_item8(a.in[14], 2 * FF, D, 224, r, F.ws + WS_WGU, true, WSC_GU, scr, lane); continue; } r -= I_GU;
;         if (r < I_DN) { tr_item8(a.in[15], D, FF, 32, r, F.ws + WS_WDN, false, WSC_DN, scr, lane); continue; } r -= I_DN;
;         if (r < NE * I_GU) { const int e = r / I_GU, rr = r % I_GU; tr_item8(a.in[18] + (size_t)e * D * 2 * FF, 2 * FF, D, 224, rr, F.ws + WS_WMGU + (size_t)e * 2 * FF * D, true, WSC_GU, scr, lane); continue; } r -= NE * I_GU;
;         { const int e = r / I_DN, rr = r % I_DN; tr_item8(a.in[19] + (size_t)e * FF * D, D, FF, 32, rr, F.ws + WS_WMDN + (size_t)e * D * FF, false, WSC_DN, scr, lane); }
;     }
; }
; __global__ void __launch_bounds__(NWAVES * 64, 2) mk_fwd(Args args) {
;     ...
;             if (att) { swa_phase((char*)lds + RING_OFF, QO, KB, VB, XN, args.in[11], args.in[13], (LAS float*)(F.lds + RING_OFF + 100 * 1024), run, 128, F.wave);
;                        convert_items(F, args, lo + NODD, CONV_NITEMS, w, 128 * NWAVES); }
.LBB0_1403:
	s_cmpk_gt_i32 s3, 0x17ff
	s_barrier
	v_mbcnt_lo_u32_b32 v4, -1, 0
	v_mbcnt_hi_u32_b32 v4, -1, v4
	s_cbranch_scc1 .LBB0_1434
	v_ashrrev_i32_e32 v28, 5, v4
	v_and_b32_e32 v38, 31, v4
	s_movk_i32 s0, 0x84
	v_lshlrev_b32_e32 v0, 2, v38
	v_mul_lo_u32 v2, v28, s0
	v_add3_u32 v29, s56, v0, v2
	v_lshlrev_b32_e32 v2, 4, v4
	v_ashrrev_i32_e32 v30, 2, v4
	v_and_b32_e32 v2, 48, v2
	v_and_b32_e32 v6, -4, v4
	v_ashrrev_i32_e32 v33, 3, v4
	v_lshlrev_b32_e32 v4, 3, v4
	s_mov_b32 s90, s37
	s_mov_b32 s89, s36
	v_mul_u32_u24_e32 v5, 0x84, v2
	v_and_b32_e32 v20, 56, v4
	v_readlane_b32 s36, v254, 5
	v_mov_b32_e32 v1, 0
	v_add3_u32 v31, s56, v5, v6
	v_mul_u32_u24_e32 v4, 0x84, v20
	v_lshlrev_b32_e32 v5, 2, v33
	v_readlane_b32 s37, v254, 6
	v_readlane_b32 s38, v254, 7
	v_readlane_b32 s39, v254, 8
	v_readlane_b32 s40, v254, 9
	v_readlane_b32 s41, v254, 10
	v_readlane_b32 s42, v254, 11
	v_readlane_b32 s43, v254, 12
	v_readlane_b32 s44, v254, 13
	v_readlane_b32 s45, v254, 14
	v_readlane_b32 s46, v254, 15
	v_readlane_b32 s47, v254, 16
	v_readlane_b32 s48, v254, 17
	v_readlane_b32 s49, v254, 18
	v_readlane_b32 s50, v254, 19
	v_readlane_b32 s51, v254, 20
	v_add3_u32 v34, s56, v4, v5
	v_lshl_add_u64 v[6:7], s[48:49], 0, v[0:1]
	v_lshl_add_u64 v[4:5], s[50:51], 0, v[0:1]
	v_lshl_add_u64 v[8:9], s[44:45], 0, v[0:1]
	v_lshl_add_u64 v[10:11], s[40:41], 0, v[0:1]
	v_lshl_add_u64 v[12:13], s[38:39], 0, v[0:1]
	v_readlane_b32 s36, v254, 36
	s_add_i32 s3, s3, 0xb200
	v_readlane_b32 s50, v254, 50
	v_readlane_b32 s51, v254, 51
	v_mov_b32_e32 v3, v1
	v_readlane_b32 s37, v254, 37
	v_readlane_b32 s38, v254, 38
	v_readlane_b32 s39, v254, 39
	v_readlane_b32 s40, v254, 40
	v_readlane_b32 s41, v254, 41
	v_readlane_b32 s42, v254, 42
	v_readlane_b32 s43, v254, 43
	v_readlane_b32 s44, v254, 44
	v_readlane_b32 s45, v254, 45
	v_readlane_b32 s46, v254, 46
	v_readlane_b32 s47, v254, 47
	v_readlane_b32 s48, v254, 48
	v_readlane_b32 s49, v254, 49
	v_lshl_add_u64 v[14:15], s[50:51], 0, v[0:1]
	v_lshlrev_b32_e32 v0, 1, v20
	s_lshl_b32 s0, s3, 1
	v_readlane_b32 s68, v254, 28
	s_mov_b32 s88, s58
	v_add_u32_e32 v32, 16, v30
	v_add_u32_e32 v35, 8, v33
	v_add_u32_e32 v36, 16, v33
	v_add_u32_e32 v37, 24, v33
	v_lshl_add_u64 v[16:17], s[26:27], 0, v[2:3]
	v_lshl_add_u64 v[18:19], s[60:61], 0, v[2:3]
	v_lshl_add_u64 v[20:21], s[62:63], 0, v[0:1]
	v_lshl_add_u64 v[22:23], s[64:65], 0, v[0:1]
	v_lshl_add_u64 v[24:25], s[84:85], 0, v[0:1]
	v_lshl_add_u64 v[26:27], s[86:87], 0, v[0:1]
	s_lshl_b32 s8, s3, 5
	s_add_i32 s9, s0, 0x1ca00
	s_mov_b32 s1, 0
	s_movk_i32 s10, 0x2000
	s_movk_i32 s11, 0x4000
	s_movk_i32 s12, 0x6000
	s_mov_b32 s13, 0x8000
	s_mov_b32 s14, 0xa000
	s_mov_b32 s15, 0xc000
	s_mov_b32 s16, 0xe000
	s_mov_b32 s17, 0x10000
	s_mov_b32 s26, 0x12000
	s_mov_b32 s27, 0x14000
	s_mov_b32 s30, 0x16000
	s_mov_b32 s31, 0x18000
	s_mov_b32 s36, 0x1a000
	s_mov_b32 s37, 0x1c000
	s_mov_b32 s38, 0x1e000
	s_mov_b32 s39, 0x20000
	s_mov_b32 s40, 0x22000
	s_mov_b32 s41, 0x24000
	s_mov_b32 s42, 0x26000
	s_mov_b32 s43, 0x28000
	s_mov_b32 s44, 0x2a000
	s_mov_b32 s45, 0x2c000
	s_mov_b32 s46, 0x2e000
	s_mov_b32 s47, 0x30000
	s_mov_b32 s48, 0x32000
	s_mov_b32 s49, 0x34000
	s_mov_b32 s50, 0x36000
	s_mov_b32 s51, 0x38000
	s_mov_b32 s52, 0x3a000
	s_mov_b32 s53, 0x3c000
	s_mov_b32 s54, 0x3e000
	s_movk_i32 s55, 0xe00
	s_movk_i32 s56, 0x7000
	s_movk_i32 s57, 0x7fff
	s_mov_b32 s58, 0xffff0000
	s_movk_i32 s59, 0x1800
	s_movk_i32 s60, 0x3040
	v_lshlrev_b32_e32 v0, 2, v38
	v_add_u32_e32 v38, 0x400, v29
	v_add_u32_e32 v39, 0x800, v29
	v_add_u32_e32 v40, 0xc00, v29
	v_add_u32_e32 v41, 0x1000, v29
	v_add_u32_e32 v42, 0x1400, v29
	v_add_u32_e32 v43, 0x1800, v29
	v_add_u32_e32 v44, 0x1c00, v29
	v_add_u32_e32 v45, 0x400, v31
	v_readlane_b32 s72, v254, 32
	v_readlane_b32 s73, v254, 33
	v_readlane_b32 s74, v254, 34
	v_readlane_b32 s75, v254, 35
	v_readlane_b32 s69, v254, 29
	v_readlane_b32 s70, v254, 30
	v_readlane_b32 s71, v254, 31
	s_branch .LBB0_1406
